# adaLN modulation phase written by hand: all 16 + 64 loads of a thread issued together (the compiler waited after every one or two), silu(c) evaluated while the weights arrive
# speedup vs baseline: 1.0168x; 1.0090x over previous
; DI void phase_mod(const Params& p, int bid, int nb, char* lds) {
;     ...
;   for (int i = tid; i < 4096; i += NT) { float v = p.c[i]; sc[i] = v / (1.f + __expf(-v)); }
;   __syncthreads();
;   float* mod = (float*)(p.ws + WS_MOD);
;   for (int g = bid; g < 384; g += nb) {
;     const int cc = tid & 15, kg = tid >> 4, col = g * 16 + cc;
;     float a0 = 0.f, a1 = 0.f, a2 = 0.f, a3 = 0.f;
; #pragma unroll 32
;     for (int k = kg; k < 1024; k += 16) { const float w = p.w_ada[(size_t)k * 6144 + col]; a0 += sc[k] * w; a1 += sc[1024 + k] * w; a2 += sc[2048 + k] * w; a3 += sc[3072 + k] * w; }
.LBB0_17:
	s_or_b64 exec, exec, s[4:5]
	s_load_dwordx16 s[36:51], s[0:1], 0x0
	v_lshrrev_b32_e32 v147, 8, v207
	v_readlane_b32 s2, v250, 0
	v_and_b32_e32 v206, 0xff, v207
	s_lshl_b32 s90, s86, 1
	v_lshl_add_u32 v176, s2, 1, v147
	s_mov_b32 s2, 0x12000
	v_mad_u32_u24 v146, v147, s2, 0
	s_movk_i32 s2, 0x180
	v_mul_u32_u24_e32 v190, 0x12000, v147
	v_mov_b32_e32 v0, v206
	v_cmp_gt_i32_e32 vcc, s2, v176
	v_readlane_b32 s3, v250, 1
	s_and_saveexec_b64 s[12:13], vcc
	s_cbranch_execz .LBB0_35
	s_waitcnt lgkmcnt(0)
	v_mov_b32_e32 v1, v206
	v_and_b32_e32 v2, 15, v1
	v_lshrrev_b32_e32 v3, 4, v1
	v_lshl_add_u32 v4, v176, 4, v2
	v_mul_u32_u24_e32 v5, 0x6000, v3
	v_lshl_add_u32 v5, v4, 2, v5
	v_lshlrev_b32_e32 v6, 2, v1
	v_lshlrev_b32_e32 v12, 2, v4
	s_add_u32 s14, s84, 0x100000
	s_addc_u32 s15, s85, 0
	global_load_dword v16, v6, s[38:39] offset:0
	global_load_dword v17, v6, s[38:39] offset:1024
	global_load_dword v18, v6, s[38:39] offset:2048
	global_load_dword v19, v6, s[38:39] offset:3072
	v_add_u32_e32 v6, 0x1000, v6
	global_load_dword v20, v6, s[38:39] offset:0
	global_load_dword v21, v6, s[38:39] offset:1024
	global_load_dword v22, v6, s[38:39] offset:2048
	global_load_dword v23, v6, s[38:39] offset:3072
	v_add_u32_e32 v6, 0x1000, v6
	global_load_dword v24, v6, s[38:39] offset:0
	global_load_dword v25, v6, s[38:39] offset:1024
	global_load_dword v26, v6, s[38:39] offset:2048
	global_load_dword v27, v6, s[38:39] offset:3072
	v_add_u32_e32 v6, 0x1000, v6
	global_load_dword v28, v6, s[38:39] offset:0
	global_load_dword v29, v6, s[38:39] offset:1024
	global_load_dword v30, v6, s[38:39] offset:2048
	global_load_dword v31, v6, s[38:39] offset:3072
	global_load_dword v32, v5, s[40:41]
	v_add_u32_e32 v8, 0x60000, v5
	global_load_dword v33, v8, s[40:41]
	v_add_u32_e32 v7, 0xc0000, v5
	global_load_dword v34, v7, s[40:41]
	v_add_u32_e32 v8, 0x120000, v5
	global_load_dword v35, v8, s[40:41]
	v_add_u32_e32 v7, 0x180000, v5
	global_load_dword v36, v7, s[40:41]
	v_add_u32_e32 v8, 0x1e0000, v5
	global_load_dword v37, v8, s[40:41]
	v_add_u32_e32 v7, 0x240000, v5
	global_load_dword v38, v7, s[40:41]
	v_add_u32_e32 v8, 0x2a0000, v5
	global_load_dword v39, v8, s[40:41]
	v_add_u32_e32 v7, 0x300000, v5
	global_load_dword v40, v7, s[40:41]
	v_add_u32_e32 v8, 0x360000, v5
	global_load_dword v41, v8, s[40:41]
	v_add_u32_e32 v7, 0x3c0000, v5
	global_load_dword v42, v7, s[40:41]
	v_add_u32_e32 v8, 0x420000, v5
	global_load_dword v43, v8, s[40:41]
	v_add_u32_e32 v7, 0x480000, v5
	global_load_dword v44, v7, s[40:41]
	v_add_u32_e32 v8, 0x4e0000, v5
	global_load_dword v45, v8, s[40:41]
	v_add_u32_e32 v7, 0x540000, v5
	global_load_dword v46, v7, s[40:41]
	v_add_u32_e32 v8, 0x5a0000, v5
	global_load_dword v47, v8, s[40:41]
	v_add_u32_e32 v7, 0x600000, v5
	global_load_dword v48, v7, s[40:41]
	v_add_u32_e32 v8, 0x660000, v5
	global_load_dword v49, v8, s[40:41]
	v_add_u32_e32 v7, 0x6c0000, v5
	global_load_dword v50, v7, s[40:41]
	v_add_u32_e32 v8, 0x720000, v5
	global_load_dword v51, v8, s[40:41]
	v_add_u32_e32 v7, 0x780000, v5
	global_load_dword v52, v7, s[40:41]
	v_add_u32_e32 v8, 0x7e0000, v5
	global_load_dword v53, v8, s[40:41]
	v_add_u32_e32 v7, 0x840000, v5
	global_load_dword v54, v7, s[40:41]
	v_add_u32_e32 v8, 0x8a0000, v5
	global_load_dword v55, v8, s[40:41]
	v_add_u32_e32 v7, 0x900000, v5
	global_load_dword v56, v7, s[40:41]
	v_add_u32_e32 v8, 0x960000, v5
	global_load_dword v57, v8, s[40:41]
	v_add_u32_e32 v7, 0x9c0000, v5
	global_load_dword v58, v7, s[40:41]
	v_add_u32_e32 v8, 0xa20000, v5
	global_load_dword v59, v8, s[40:41]
	v_add_u32_e32 v7, 0xa80000, v5
	global_load_dword v60, v7, s[40:41]
	v_add_u32_e32 v8, 0xae0000, v5
	global_load_dword v61, v8, s[40:41]
	v_add_u32_e32 v7, 0xb40000, v5
	global_load_dword v62, v7, s[40:41]
	v_add_u32_e32 v8, 0xba0000, v5
	global_load_dword v63, v8, s[40:41]
	v_add_u32_e32 v7, 0xc00000, v5
	global_load_dword v64, v7, s[40:41]
	v_add_u32_e32 v8, 0xc60000, v5
	global_load_dword v65, v8, s[40:41]
	v_add_u32_e32 v7, 0xcc0000, v5
	global_load_dword v66, v7, s[40:41]
	v_add_u32_e32 v8, 0xd20000, v5
	global_load_dword v67, v8, s[40:41]
	v_add_u32_e32 v7, 0xd80000, v5
	global_load_dword v68, v7, s[40:41]
	v_add_u32_e32 v8, 0xde0000, v5
	global_load_dword v69, v8, s[40:41]
	v_add_u32_e32 v7, 0xe40000, v5
	global_load_dword v70, v7, s[40:41]
	v_add_u32_e32 v8, 0xea0000, v5
	global_load_dword v71, v8, s[40:41]
	v_add_u32_e32 v7, 0xf00000, v5
	global_load_dword v72, v7, s[40:41]
	v_add_u32_e32 v8, 0xf60000, v5
	global_load_dword v73, v8, s[40:41]
	v_add_u32_e32 v7, 0xfc0000, v5
	global_load_dword v74, v7, s[40:41]
	v_add_u32_e32 v8, 0x1020000, v5
	global_load_dword v75, v8, s[40:41]
	v_add_u32_e32 v7, 0x1080000, v5
	global_load_dword v76, v7, s[40:41]
	v_add_u32_e32 v8, 0x10e0000, v5
	global_load_dword v77, v8, s[40:41]
	v_lshl_add_u32 v9, v1, 2, v190
	s_waitcnt vmcnt(61)
	v_mul_f32_e32 v132, 0xbfb8aa3b, v16
	v_exp_f32_e32 v132, v132
	s_nop 0
	v_add_f32_e32 v132, 1.0, v132
	v_div_scale_f32 v133, s[10:11], v132, v132, v16
	v_rcp_f32_e32 v134, v133
	v_div_scale_f32 v135, vcc, v16, v132, v16
	v_fma_f32 v136, -v133, v134, 1.0
	v_fmac_f32_e32 v134, v136, v134
	v_mul_f32_e32 v136, v135, v134
	v_fma_f32 v137, -v133, v136, v135
	v_fmac_f32_e32 v136, v137, v134
	v_fma_f32 v133, -v133, v136, v135
	v_div_fmas_f32 v133, v133, v134, v136
	v_div_fixup_f32 v16, v133, v132, v16
	ds_write_b32 v9, v16 offset:0
	s_waitcnt vmcnt(60)
; DI void phase_mod(const Params& p, int bid, int nb, char* lds) {
;     ...
;   for (int i = tid; i < 4096; i += NT) { float v = p.c[i]; sc[i] = v / (1.f + __expf(-v)); }
	v_mul_f32_e32 v132, 0xbfb8aa3b, v17
	v_exp_f32_e32 v132, v132
	s_nop 0
	v_add_f32_e32 v132, 1.0, v132
	v_div_scale_f32 v133, s[10:11], v132, v132, v17
	v_rcp_f32_e32 v134, v133
	v_div_scale_f32 v135, vcc, v17, v132, v17
	v_fma_f32 v136, -v133, v134, 1.0
	v_fmac_f32_e32 v134, v136, v134
	v_mul_f32_e32 v136, v135, v134
	v_fma_f32 v137, -v133, v136, v135
	v_fmac_f32_e32 v136, v137, v134
	v_fma_f32 v133, -v133, v136, v135
	v_div_fmas_f32 v133, v133, v134, v136
	v_div_fixup_f32 v17, v133, v132, v17
	ds_write_b32 v9, v17 offset:1024
	s_waitcnt vmcnt(59)
	v_mul_f32_e32 v132, 0xbfb8aa3b, v18
	v_exp_f32_e32 v132, v132
	s_nop 0
	v_add_f32_e32 v132, 1.0, v132
	v_div_scale_f32 v133, s[10:11], v132, v132, v18
	v_rcp_f32_e32 v134, v133
	v_div_scale_f32 v135, vcc, v18, v132, v18
	v_fma_f32 v136, -v133, v134, 1.0
	v_fmac_f32_e32 v134, v136, v134
	v_mul_f32_e32 v136, v135, v134
	v_fma_f32 v137, -v133, v136, v135
	v_fmac_f32_e32 v136, v137, v134
	v_fma_f32 v133, -v133, v136, v135
	v_div_fmas_f32 v133, v133, v134, v136
	v_div_fixup_f32 v18, v133, v132, v18
	ds_write_b32 v9, v18 offset:2048
	s_waitcnt vmcnt(58)
	v_mul_f32_e32 v132, 0xbfb8aa3b, v19
	v_exp_f32_e32 v132, v132
	s_nop 0
	v_add_f32_e32 v132, 1.0, v132
	v_div_scale_f32 v133, s[10:11], v132, v132, v19
	v_rcp_f32_e32 v134, v133
	v_div_scale_f32 v135, vcc, v19, v132, v19
	v_fma_f32 v136, -v133, v134, 1.0
	v_fmac_f32_e32 v134, v136, v134
	v_mul_f32_e32 v136, v135, v134
	v_fma_f32 v137, -v133, v136, v135
	v_fmac_f32_e32 v136, v137, v134
	v_fma_f32 v133, -v133, v136, v135
	v_div_fmas_f32 v133, v133, v134, v136
	v_div_fixup_f32 v19, v133, v132, v19
	ds_write_b32 v9, v19 offset:3072
	s_waitcnt vmcnt(57)
	v_mul_f32_e32 v132, 0xbfb8aa3b, v20
	v_exp_f32_e32 v132, v132
	s_nop 0
	v_add_f32_e32 v132, 1.0, v132
	v_div_scale_f32 v133, s[10:11], v132, v132, v20
	v_rcp_f32_e32 v134, v133
	v_div_scale_f32 v135, vcc, v20, v132, v20
	v_fma_f32 v136, -v133, v134, 1.0
	v_fmac_f32_e32 v134, v136, v134
	v_mul_f32_e32 v136, v135, v134
	v_fma_f32 v137, -v133, v136, v135
	v_fmac_f32_e32 v136, v137, v134
	v_fma_f32 v133, -v133, v136, v135
	v_div_fmas_f32 v133, v133, v134, v136
	v_div_fixup_f32 v20, v133, v132, v20
	ds_write_b32 v9, v20 offset:4096
	s_waitcnt vmcnt(56)
	v_mul_f32_e32 v132, 0xbfb8aa3b, v21
	v_exp_f32_e32 v132, v132
	s_nop 0
	v_add_f32_e32 v132, 1.0, v132
	v_div_scale_f32 v133, s[10:11], v132, v132, v21
	v_rcp_f32_e32 v134, v133
	v_div_scale_f32 v135, vcc, v21, v132, v21
	v_fma_f32 v136, -v133, v134, 1.0
	v_fmac_f32_e32 v134, v136, v134
	v_mul_f32_e32 v136, v135, v134
	v_fma_f32 v137, -v133, v136, v135
	v_fmac_f32_e32 v136, v137, v134
	v_fma_f32 v133, -v133, v136, v135
	v_div_fmas_f32 v133, v133, v134, v136
	v_div_fixup_f32 v21, v133, v132, v21
	ds_write_b32 v9, v21 offset:5120
	s_waitcnt vmcnt(55)
	v_mul_f32_e32 v132, 0xbfb8aa3b, v22
	v_exp_f32_e32 v132, v132
	s_nop 0
	v_add_f32_e32 v132, 1.0, v132
	v_div_scale_f32 v133, s[10:11], v132, v132, v22
	v_rcp_f32_e32 v134, v133
	v_div_scale_f32 v135, vcc, v22, v132, v22
	v_fma_f32 v136, -v133, v134, 1.0
	v_fmac_f32_e32 v134, v136, v134
	v_mul_f32_e32 v136, v135, v134
	v_fma_f32 v137, -v133, v136, v135
	v_fmac_f32_e32 v136, v137, v134
	v_fma_f32 v133, -v133, v136, v135
	v_div_fmas_f32 v133, v133, v134, v136
	v_div_fixup_f32 v22, v133, v132, v22
	ds_write_b32 v9, v22 offset:6144
	s_waitcnt vmcnt(54)
	v_mul_f32_e32 v132, 0xbfb8aa3b, v23
	v_exp_f32_e32 v132, v132
	s_nop 0
	v_add_f32_e32 v132, 1.0, v132
	v_div_scale_f32 v133, s[10:11], v132, v132, v23
	v_rcp_f32_e32 v134, v133
	v_div_scale_f32 v135, vcc, v23, v132, v23
	v_fma_f32 v136, -v133, v134, 1.0
	v_fmac_f32_e32 v134, v136, v134
	v_mul_f32_e32 v136, v135, v134
	v_fma_f32 v137, -v133, v136, v135
	v_fmac_f32_e32 v136, v137, v134
	v_fma_f32 v133, -v133, v136, v135
	v_div_fmas_f32 v133, v133, v134, v136
	v_div_fixup_f32 v23, v133, v132, v23
	ds_write_b32 v9, v23 offset:7168
	s_waitcnt vmcnt(53)
	v_mul_f32_e32 v132, 0xbfb8aa3b, v24
	v_exp_f32_e32 v132, v132
	s_nop 0
	v_add_f32_e32 v132, 1.0, v132
	v_div_scale_f32 v133, s[10:11], v132, v132, v24
	v_rcp_f32_e32 v134, v133
	v_div_scale_f32 v135, vcc, v24, v132, v24
	v_fma_f32 v136, -v133, v134, 1.0
	v_fmac_f32_e32 v134, v136, v134
	v_mul_f32_e32 v136, v135, v134
	v_fma_f32 v137, -v133, v136, v135
	v_fmac_f32_e32 v136, v137, v134
	v_fma_f32 v133, -v133, v136, v135
	v_div_fmas_f32 v133, v133, v134, v136
	v_div_fixup_f32 v24, v133, v132, v24
	ds_write_b32 v9, v24 offset:8192
	s_waitcnt vmcnt(52)
	v_mul_f32_e32 v132, 0xbfb8aa3b, v25
	v_exp_f32_e32 v132, v132
	s_nop 0
	v_add_f32_e32 v132, 1.0, v132
	v_div_scale_f32 v133, s[10:11], v132, v132, v25
	v_rcp_f32_e32 v134, v133
	v_div_scale_f32 v135, vcc, v25, v132, v25
	v_fma_f32 v136, -v133, v134, 1.0
	v_fmac_f32_e32 v134, v136, v134
	v_mul_f32_e32 v136, v135, v134
	v_fma_f32 v137, -v133, v136, v135
	v_fmac_f32_e32 v136, v137, v134
	v_fma_f32 v133, -v133, v136, v135
	v_div_fmas_f32 v133, v133, v134, v136
	v_div_fixup_f32 v25, v133, v132, v25
	ds_write_b32 v9, v25 offset:9216
	s_waitcnt vmcnt(51)
	v_mul_f32_e32 v132, 0xbfb8aa3b, v26
	v_exp_f32_e32 v132, v132
	s_nop 0
	v_add_f32_e32 v132, 1.0, v132
	v_div_scale_f32 v133, s[10:11], v132, v132, v26
	v_rcp_f32_e32 v134, v133
	v_div_scale_f32 v135, vcc, v26, v132, v26
	v_fma_f32 v136, -v133, v134, 1.0
	v_fmac_f32_e32 v134, v136, v134
	v_mul_f32_e32 v136, v135, v134
	v_fma_f32 v137, -v133, v136, v135
	v_fmac_f32_e32 v136, v137, v134
	v_fma_f32 v133, -v133, v136, v135
	v_div_fmas_f32 v133, v133, v134, v136
	v_div_fixup_f32 v26, v133, v132, v26
	ds_write_b32 v9, v26 offset:10240
	s_waitcnt vmcnt(50)
; DI void phase_mod(const Params& p, int bid, int nb, char* lds) {
;     ...
;   for (int i = tid; i < 4096; i += NT) { float v = p.c[i]; sc[i] = v / (1.f + __expf(-v)); }
;   __syncthreads();
;   float* mod = (float*)(p.ws + WS_MOD);
;   for (int g = bid; g < 384; g += nb) {
;     const int cc = tid & 15, kg = tid >> 4, col = g * 16 + cc;
;     float a0 = 0.f, a1 = 0.f, a2 = 0.f, a3 = 0.f;
; #pragma unroll 32
;     for (int k = kg; k < 1024; k += 16) { const float w = p.w_ada[(size_t)k * 6144 + col]; a0 += sc[k] * w; a1 += sc[1024 + k] * w; a2 += sc[2048 + k] * w; a3 += sc[3072 + k] * w; }
	v_mul_f32_e32 v132, 0xbfb8aa3b, v27
	v_exp_f32_e32 v132, v132
	s_nop 0
	v_add_f32_e32 v132, 1.0, v132
	v_div_scale_f32 v133, s[10:11], v132, v132, v27
	v_rcp_f32_e32 v134, v133
	v_div_scale_f32 v135, vcc, v27, v132, v27
	v_fma_f32 v136, -v133, v134, 1.0
	v_fmac_f32_e32 v134, v136, v134
	v_mul_f32_e32 v136, v135, v134
	v_fma_f32 v137, -v133, v136, v135
	v_fmac_f32_e32 v136, v137, v134
	v_fma_f32 v133, -v133, v136, v135
	v_div_fmas_f32 v133, v133, v134, v136
	v_div_fixup_f32 v27, v133, v132, v27
	ds_write_b32 v9, v27 offset:11264
	s_waitcnt vmcnt(49)
	v_mul_f32_e32 v132, 0xbfb8aa3b, v28
	v_exp_f32_e32 v132, v132
	s_nop 0
	v_add_f32_e32 v132, 1.0, v132
	v_div_scale_f32 v133, s[10:11], v132, v132, v28
	v_rcp_f32_e32 v134, v133
	v_div_scale_f32 v135, vcc, v28, v132, v28
	v_fma_f32 v136, -v133, v134, 1.0
	v_fmac_f32_e32 v134, v136, v134
	v_mul_f32_e32 v136, v135, v134
	v_fma_f32 v137, -v133, v136, v135
	v_fmac_f32_e32 v136, v137, v134
	v_fma_f32 v133, -v133, v136, v135
	v_div_fmas_f32 v133, v133, v134, v136
	v_div_fixup_f32 v28, v133, v132, v28
	ds_write_b32 v9, v28 offset:12288
	s_waitcnt vmcnt(48)
	v_mul_f32_e32 v132, 0xbfb8aa3b, v29
	v_exp_f32_e32 v132, v132
	s_nop 0
	v_add_f32_e32 v132, 1.0, v132
	v_div_scale_f32 v133, s[10:11], v132, v132, v29
	v_rcp_f32_e32 v134, v133
	v_div_scale_f32 v135, vcc, v29, v132, v29
	v_fma_f32 v136, -v133, v134, 1.0
	v_fmac_f32_e32 v134, v136, v134
	v_mul_f32_e32 v136, v135, v134
	v_fma_f32 v137, -v133, v136, v135
	v_fmac_f32_e32 v136, v137, v134
	v_fma_f32 v133, -v133, v136, v135
	v_div_fmas_f32 v133, v133, v134, v136
	v_div_fixup_f32 v29, v133, v132, v29
	ds_write_b32 v9, v29 offset:13312
	s_waitcnt vmcnt(47)
	v_mul_f32_e32 v132, 0xbfb8aa3b, v30
	v_exp_f32_e32 v132, v132
	s_nop 0
	v_add_f32_e32 v132, 1.0, v132
	v_div_scale_f32 v133, s[10:11], v132, v132, v30
	v_rcp_f32_e32 v134, v133
	v_div_scale_f32 v135, vcc, v30, v132, v30
	v_fma_f32 v136, -v133, v134, 1.0
	v_fmac_f32_e32 v134, v136, v134
	v_mul_f32_e32 v136, v135, v134
	v_fma_f32 v137, -v133, v136, v135
	v_fmac_f32_e32 v136, v137, v134
	v_fma_f32 v133, -v133, v136, v135
	v_div_fmas_f32 v133, v133, v134, v136
	v_div_fixup_f32 v30, v133, v132, v30
	ds_write_b32 v9, v30 offset:14336
	s_waitcnt vmcnt(46)
	v_mul_f32_e32 v132, 0xbfb8aa3b, v31
	v_exp_f32_e32 v132, v132
	s_nop 0
	v_add_f32_e32 v132, 1.0, v132
	v_div_scale_f32 v133, s[10:11], v132, v132, v31
	v_rcp_f32_e32 v134, v133
	v_div_scale_f32 v135, vcc, v31, v132, v31
	v_fma_f32 v136, -v133, v134, 1.0
	v_fmac_f32_e32 v134, v136, v134
	v_mul_f32_e32 v136, v135, v134
	v_fma_f32 v137, -v133, v136, v135
	v_fmac_f32_e32 v136, v137, v134
	v_fma_f32 v133, -v133, v136, v135
	v_div_fmas_f32 v133, v133, v134, v136
	v_div_fixup_f32 v31, v133, v132, v31
	ds_write_b32 v9, v31 offset:15360
	v_add_u32_e32 v7, 0x1140000, v5
	global_load_dword v78, v7, s[40:41]
	v_add_u32_e32 v8, 0x11a0000, v5
	global_load_dword v79, v8, s[40:41]
	v_add_u32_e32 v7, 0x1200000, v5
	global_load_dword v80, v7, s[40:41]
	v_add_u32_e32 v8, 0x1260000, v5
	global_load_dword v81, v8, s[40:41]
	v_add_u32_e32 v7, 0x12c0000, v5
	global_load_dword v82, v7, s[40:41]
	v_add_u32_e32 v8, 0x1320000, v5
	global_load_dword v83, v8, s[40:41]
	v_add_u32_e32 v7, 0x1380000, v5
	global_load_dword v84, v7, s[40:41]
	v_add_u32_e32 v8, 0x13e0000, v5
	global_load_dword v85, v8, s[40:41]
	v_add_u32_e32 v7, 0x1440000, v5
	global_load_dword v86, v7, s[40:41]
	v_add_u32_e32 v8, 0x14a0000, v5
	global_load_dword v87, v8, s[40:41]
	v_add_u32_e32 v7, 0x1500000, v5
	global_load_dword v88, v7, s[40:41]
	v_add_u32_e32 v8, 0x1560000, v5
	global_load_dword v89, v8, s[40:41]
	v_add_u32_e32 v7, 0x15c0000, v5
	global_load_dword v90, v7, s[40:41]
	v_add_u32_e32 v8, 0x1620000, v5
	global_load_dword v91, v8, s[40:41]
	v_add_u32_e32 v7, 0x1680000, v5
	global_load_dword v92, v7, s[40:41]
	v_add_u32_e32 v8, 0x16e0000, v5
	global_load_dword v93, v8, s[40:41]
	v_add_u32_e32 v7, 0x1740000, v5
	global_load_dword v94, v7, s[40:41]
	v_add_u32_e32 v8, 0x17a0000, v5
	global_load_dword v95, v8, s[40:41]
	global_load_dword v10, v12, s[42:43]
	s_waitcnt lgkmcnt(0)
	s_barrier
	v_lshl_add_u32 v9, v3, 2, v190
	v_mov_b32_e32 v96, 0
	v_mov_b32_e32 v97, 0
	v_mov_b32_e32 v98, 0
	v_mov_b32_e32 v99, 0
	ds_read2st64_b32 v[100:101], v9 offset1:16
	ds_read2st64_b32 v[102:103], v9 offset0:32 offset1:48
	v_add_u32_e32 v9, 64, v9
	ds_read2st64_b32 v[104:105], v9 offset1:16
	ds_read2st64_b32 v[106:107], v9 offset0:32 offset1:48
	v_add_u32_e32 v9, 64, v9
	ds_read2st64_b32 v[108:109], v9 offset1:16
	ds_read2st64_b32 v[110:111], v9 offset0:32 offset1:48
	v_add_u32_e32 v9, 64, v9
	ds_read2st64_b32 v[112:113], v9 offset1:16
	ds_read2st64_b32 v[114:115], v9 offset0:32 offset1:48
	v_add_u32_e32 v9, 64, v9
	ds_read2st64_b32 v[116:117], v9 offset1:16
	ds_read2st64_b32 v[118:119], v9 offset0:32 offset1:48
	v_add_u32_e32 v9, 64, v9
	ds_read2st64_b32 v[120:121], v9 offset1:16
	ds_read2st64_b32 v[122:123], v9 offset0:32 offset1:48
	v_add_u32_e32 v9, 64, v9
	s_waitcnt vmcnt(63) lgkmcnt(10)
	v_fmac_f32_e32 v96, v32, v100
	v_fmac_f32_e32 v97, v32, v101
	v_fmac_f32_e32 v98, v32, v102
	v_fmac_f32_e32 v99, v32, v103
	ds_read2st64_b32 v[124:125], v9 offset1:16
	ds_read2st64_b32 v[126:127], v9 offset0:32 offset1:48
	v_add_u32_e32 v9, 64, v9
	s_waitcnt vmcnt(63) lgkmcnt(10)
	v_fmac_f32_e32 v96, v33, v104
	v_fmac_f32_e32 v97, v33, v105
	v_fmac_f32_e32 v98, v33, v106
	v_fmac_f32_e32 v99, v33, v107
	ds_read2st64_b32 v[128:129], v9 offset1:16
	ds_read2st64_b32 v[130:131], v9 offset0:32 offset1:48
	v_add_u32_e32 v9, 64, v9
	s_waitcnt vmcnt(62) lgkmcnt(10)
; DI void phase_mod(const Params& p, int bid, int nb, char* lds) {
;     ...
;     for (int k = kg; k < 1024; k += 16) { const float w = p.w_ada[(size_t)k * 6144 + col]; a0 += sc[k] * w; a1 += sc[1024 + k] * w; a2 += sc[2048 + k] * w; a3 += sc[3072 + k] * w; }
	v_fmac_f32_e32 v96, v34, v108
	v_fmac_f32_e32 v97, v34, v109
	v_fmac_f32_e32 v98, v34, v110
	v_fmac_f32_e32 v99, v34, v111
	ds_read2st64_b32 v[100:101], v9 offset1:16
	ds_read2st64_b32 v[102:103], v9 offset0:32 offset1:48
	v_add_u32_e32 v9, 64, v9
	s_waitcnt vmcnt(61) lgkmcnt(10)
	v_fmac_f32_e32 v96, v35, v112
	v_fmac_f32_e32 v97, v35, v113
	v_fmac_f32_e32 v98, v35, v114
	v_fmac_f32_e32 v99, v35, v115
	ds_read2st64_b32 v[104:105], v9 offset1:16
	ds_read2st64_b32 v[106:107], v9 offset0:32 offset1:48
	v_add_u32_e32 v9, 64, v9
	s_waitcnt vmcnt(60) lgkmcnt(10)
	v_fmac_f32_e32 v96, v36, v116
	v_fmac_f32_e32 v97, v36, v117
	v_fmac_f32_e32 v98, v36, v118
	v_fmac_f32_e32 v99, v36, v119
	ds_read2st64_b32 v[108:109], v9 offset1:16
	ds_read2st64_b32 v[110:111], v9 offset0:32 offset1:48
	v_add_u32_e32 v9, 64, v9
	s_waitcnt vmcnt(59) lgkmcnt(10)
	v_fmac_f32_e32 v96, v37, v120
	v_fmac_f32_e32 v97, v37, v121
	v_fmac_f32_e32 v98, v37, v122
	v_fmac_f32_e32 v99, v37, v123
	ds_read2st64_b32 v[112:113], v9 offset1:16
	ds_read2st64_b32 v[114:115], v9 offset0:32 offset1:48
	v_add_u32_e32 v9, 64, v9
	s_waitcnt vmcnt(58) lgkmcnt(10)
	v_fmac_f32_e32 v96, v38, v124
	v_fmac_f32_e32 v97, v38, v125
	v_fmac_f32_e32 v98, v38, v126
	v_fmac_f32_e32 v99, v38, v127
	ds_read2st64_b32 v[116:117], v9 offset1:16
	ds_read2st64_b32 v[118:119], v9 offset0:32 offset1:48
	v_add_u32_e32 v9, 64, v9
	s_waitcnt vmcnt(57) lgkmcnt(10)
	v_fmac_f32_e32 v96, v39, v128
	v_fmac_f32_e32 v97, v39, v129
	v_fmac_f32_e32 v98, v39, v130
	v_fmac_f32_e32 v99, v39, v131
	ds_read2st64_b32 v[120:121], v9 offset1:16
	ds_read2st64_b32 v[122:123], v9 offset0:32 offset1:48
	v_add_u32_e32 v9, 64, v9
	s_waitcnt vmcnt(56) lgkmcnt(10)
	v_fmac_f32_e32 v96, v40, v100
	v_fmac_f32_e32 v97, v40, v101
	v_fmac_f32_e32 v98, v40, v102
	v_fmac_f32_e32 v99, v40, v103
	ds_read2st64_b32 v[124:125], v9 offset1:16
	ds_read2st64_b32 v[126:127], v9 offset0:32 offset1:48
	v_add_u32_e32 v9, 64, v9
	s_waitcnt vmcnt(55) lgkmcnt(10)
	v_fmac_f32_e32 v96, v41, v104
	v_fmac_f32_e32 v97, v41, v105
	v_fmac_f32_e32 v98, v41, v106
	v_fmac_f32_e32 v99, v41, v107
	ds_read2st64_b32 v[128:129], v9 offset1:16
	ds_read2st64_b32 v[130:131], v9 offset0:32 offset1:48
	v_add_u32_e32 v9, 64, v9
	s_waitcnt vmcnt(54) lgkmcnt(10)
	v_fmac_f32_e32 v96, v42, v108
	v_fmac_f32_e32 v97, v42, v109
	v_fmac_f32_e32 v98, v42, v110
	v_fmac_f32_e32 v99, v42, v111
	ds_read2st64_b32 v[100:101], v9 offset1:16
	ds_read2st64_b32 v[102:103], v9 offset0:32 offset1:48
	v_add_u32_e32 v9, 64, v9
	s_waitcnt vmcnt(53) lgkmcnt(10)
	v_fmac_f32_e32 v96, v43, v112
	v_fmac_f32_e32 v97, v43, v113
	v_fmac_f32_e32 v98, v43, v114
	v_fmac_f32_e32 v99, v43, v115
	ds_read2st64_b32 v[104:105], v9 offset1:16
	ds_read2st64_b32 v[106:107], v9 offset0:32 offset1:48
	v_add_u32_e32 v9, 64, v9
	s_waitcnt vmcnt(52) lgkmcnt(10)
	v_fmac_f32_e32 v96, v44, v116
	v_fmac_f32_e32 v97, v44, v117
	v_fmac_f32_e32 v98, v44, v118
	v_fmac_f32_e32 v99, v44, v119
	ds_read2st64_b32 v[108:109], v9 offset1:16
	ds_read2st64_b32 v[110:111], v9 offset0:32 offset1:48
	v_add_u32_e32 v9, 64, v9
	s_waitcnt vmcnt(51) lgkmcnt(10)
	v_fmac_f32_e32 v96, v45, v120
	v_fmac_f32_e32 v97, v45, v121
	v_fmac_f32_e32 v98, v45, v122
	v_fmac_f32_e32 v99, v45, v123
	ds_read2st64_b32 v[112:113], v9 offset1:16
	ds_read2st64_b32 v[114:115], v9 offset0:32 offset1:48
	v_add_u32_e32 v9, 64, v9
	s_waitcnt vmcnt(50) lgkmcnt(10)
	v_fmac_f32_e32 v96, v46, v124
	v_fmac_f32_e32 v97, v46, v125
	v_fmac_f32_e32 v98, v46, v126
	v_fmac_f32_e32 v99, v46, v127
	ds_read2st64_b32 v[116:117], v9 offset1:16
	ds_read2st64_b32 v[118:119], v9 offset0:32 offset1:48
	v_add_u32_e32 v9, 64, v9
	s_waitcnt vmcnt(49) lgkmcnt(10)
	v_fmac_f32_e32 v96, v47, v128
	v_fmac_f32_e32 v97, v47, v129
	v_fmac_f32_e32 v98, v47, v130
	v_fmac_f32_e32 v99, v47, v131
	ds_read2st64_b32 v[120:121], v9 offset1:16
	ds_read2st64_b32 v[122:123], v9 offset0:32 offset1:48
	v_add_u32_e32 v9, 64, v9
	s_waitcnt vmcnt(48) lgkmcnt(10)
	v_fmac_f32_e32 v96, v48, v100
	v_fmac_f32_e32 v97, v48, v101
	v_fmac_f32_e32 v98, v48, v102
	v_fmac_f32_e32 v99, v48, v103
	ds_read2st64_b32 v[124:125], v9 offset1:16
	ds_read2st64_b32 v[126:127], v9 offset0:32 offset1:48
	v_add_u32_e32 v9, 64, v9
	s_waitcnt vmcnt(47) lgkmcnt(10)
	v_fmac_f32_e32 v96, v49, v104
	v_fmac_f32_e32 v97, v49, v105
	v_fmac_f32_e32 v98, v49, v106
	v_fmac_f32_e32 v99, v49, v107
	ds_read2st64_b32 v[128:129], v9 offset1:16
	ds_read2st64_b32 v[130:131], v9 offset0:32 offset1:48
	v_add_u32_e32 v9, 64, v9
	s_waitcnt vmcnt(46) lgkmcnt(10)
	v_fmac_f32_e32 v96, v50, v108
	v_fmac_f32_e32 v97, v50, v109
	v_fmac_f32_e32 v98, v50, v110
	v_fmac_f32_e32 v99, v50, v111
	ds_read2st64_b32 v[100:101], v9 offset1:16
	ds_read2st64_b32 v[102:103], v9 offset0:32 offset1:48
	v_add_u32_e32 v9, 64, v9
	s_waitcnt vmcnt(45) lgkmcnt(10)
	v_fmac_f32_e32 v96, v51, v112
	v_fmac_f32_e32 v97, v51, v113
	v_fmac_f32_e32 v98, v51, v114
	v_fmac_f32_e32 v99, v51, v115
	ds_read2st64_b32 v[104:105], v9 offset1:16
	ds_read2st64_b32 v[106:107], v9 offset0:32 offset1:48
	v_add_u32_e32 v9, 64, v9
	s_waitcnt vmcnt(44) lgkmcnt(10)
	v_fmac_f32_e32 v96, v52, v116
	v_fmac_f32_e32 v97, v52, v117
	v_fmac_f32_e32 v98, v52, v118
	v_fmac_f32_e32 v99, v52, v119
	ds_read2st64_b32 v[108:109], v9 offset1:16
	ds_read2st64_b32 v[110:111], v9 offset0:32 offset1:48
	v_add_u32_e32 v9, 64, v9
	s_waitcnt vmcnt(43) lgkmcnt(10)
	v_fmac_f32_e32 v96, v53, v120
	v_fmac_f32_e32 v97, v53, v121
	v_fmac_f32_e32 v98, v53, v122
	v_fmac_f32_e32 v99, v53, v123
	ds_read2st64_b32 v[112:113], v9 offset1:16
	ds_read2st64_b32 v[114:115], v9 offset0:32 offset1:48
	v_add_u32_e32 v9, 64, v9
	s_waitcnt vmcnt(42) lgkmcnt(10)
; DI void phase_mod(const Params& p, int bid, int nb, char* lds) {
;     ...
;     for (int k = kg; k < 1024; k += 16) { const float w = p.w_ada[(size_t)k * 6144 + col]; a0 += sc[k] * w; a1 += sc[1024 + k] * w; a2 += sc[2048 + k] * w; a3 += sc[3072 + k] * w; }
	v_fmac_f32_e32 v96, v54, v124
	v_fmac_f32_e32 v97, v54, v125
	v_fmac_f32_e32 v98, v54, v126
	v_fmac_f32_e32 v99, v54, v127
	ds_read2st64_b32 v[116:117], v9 offset1:16
	ds_read2st64_b32 v[118:119], v9 offset0:32 offset1:48
	v_add_u32_e32 v9, 64, v9
	s_waitcnt vmcnt(41) lgkmcnt(10)
	v_fmac_f32_e32 v96, v55, v128
	v_fmac_f32_e32 v97, v55, v129
	v_fmac_f32_e32 v98, v55, v130
	v_fmac_f32_e32 v99, v55, v131
	ds_read2st64_b32 v[120:121], v9 offset1:16
	ds_read2st64_b32 v[122:123], v9 offset0:32 offset1:48
	v_add_u32_e32 v9, 64, v9
	s_waitcnt vmcnt(40) lgkmcnt(10)
	v_fmac_f32_e32 v96, v56, v100
	v_fmac_f32_e32 v97, v56, v101
	v_fmac_f32_e32 v98, v56, v102
	v_fmac_f32_e32 v99, v56, v103
	ds_read2st64_b32 v[124:125], v9 offset1:16
	ds_read2st64_b32 v[126:127], v9 offset0:32 offset1:48
	v_add_u32_e32 v9, 64, v9
	s_waitcnt vmcnt(39) lgkmcnt(10)
	v_fmac_f32_e32 v96, v57, v104
	v_fmac_f32_e32 v97, v57, v105
	v_fmac_f32_e32 v98, v57, v106
	v_fmac_f32_e32 v99, v57, v107
	ds_read2st64_b32 v[128:129], v9 offset1:16
	ds_read2st64_b32 v[130:131], v9 offset0:32 offset1:48
	v_add_u32_e32 v9, 64, v9
	s_waitcnt vmcnt(38) lgkmcnt(10)
	v_fmac_f32_e32 v96, v58, v108
	v_fmac_f32_e32 v97, v58, v109
	v_fmac_f32_e32 v98, v58, v110
	v_fmac_f32_e32 v99, v58, v111
	ds_read2st64_b32 v[100:101], v9 offset1:16
	ds_read2st64_b32 v[102:103], v9 offset0:32 offset1:48
	v_add_u32_e32 v9, 64, v9
	s_waitcnt vmcnt(37) lgkmcnt(10)
	v_fmac_f32_e32 v96, v59, v112
	v_fmac_f32_e32 v97, v59, v113
	v_fmac_f32_e32 v98, v59, v114
	v_fmac_f32_e32 v99, v59, v115
	ds_read2st64_b32 v[104:105], v9 offset1:16
	ds_read2st64_b32 v[106:107], v9 offset0:32 offset1:48
	v_add_u32_e32 v9, 64, v9
	s_waitcnt vmcnt(36) lgkmcnt(10)
	v_fmac_f32_e32 v96, v60, v116
	v_fmac_f32_e32 v97, v60, v117
	v_fmac_f32_e32 v98, v60, v118
	v_fmac_f32_e32 v99, v60, v119
	ds_read2st64_b32 v[108:109], v9 offset1:16
	ds_read2st64_b32 v[110:111], v9 offset0:32 offset1:48
	v_add_u32_e32 v9, 64, v9
	s_waitcnt vmcnt(35) lgkmcnt(10)
	v_fmac_f32_e32 v96, v61, v120
	v_fmac_f32_e32 v97, v61, v121
	v_fmac_f32_e32 v98, v61, v122
	v_fmac_f32_e32 v99, v61, v123
	ds_read2st64_b32 v[112:113], v9 offset1:16
	ds_read2st64_b32 v[114:115], v9 offset0:32 offset1:48
	v_add_u32_e32 v9, 64, v9
	s_waitcnt vmcnt(34) lgkmcnt(10)
	v_fmac_f32_e32 v96, v62, v124
	v_fmac_f32_e32 v97, v62, v125
	v_fmac_f32_e32 v98, v62, v126
	v_fmac_f32_e32 v99, v62, v127
	ds_read2st64_b32 v[116:117], v9 offset1:16
	ds_read2st64_b32 v[118:119], v9 offset0:32 offset1:48
	v_add_u32_e32 v9, 64, v9
	s_waitcnt vmcnt(33) lgkmcnt(10)
	v_fmac_f32_e32 v96, v63, v128
	v_fmac_f32_e32 v97, v63, v129
	v_fmac_f32_e32 v98, v63, v130
	v_fmac_f32_e32 v99, v63, v131
	ds_read2st64_b32 v[120:121], v9 offset1:16
	ds_read2st64_b32 v[122:123], v9 offset0:32 offset1:48
	v_add_u32_e32 v9, 64, v9
	s_waitcnt vmcnt(32) lgkmcnt(10)
	v_fmac_f32_e32 v96, v64, v100
	v_fmac_f32_e32 v97, v64, v101
	v_fmac_f32_e32 v98, v64, v102
	v_fmac_f32_e32 v99, v64, v103
	ds_read2st64_b32 v[124:125], v9 offset1:16
	ds_read2st64_b32 v[126:127], v9 offset0:32 offset1:48
	v_add_u32_e32 v9, 64, v9
	s_waitcnt vmcnt(31) lgkmcnt(10)
	v_fmac_f32_e32 v96, v65, v104
	v_fmac_f32_e32 v97, v65, v105
	v_fmac_f32_e32 v98, v65, v106
	v_fmac_f32_e32 v99, v65, v107
	ds_read2st64_b32 v[128:129], v9 offset1:16
	ds_read2st64_b32 v[130:131], v9 offset0:32 offset1:48
	v_add_u32_e32 v9, 64, v9
	s_waitcnt vmcnt(30) lgkmcnt(10)
	v_fmac_f32_e32 v96, v66, v108
	v_fmac_f32_e32 v97, v66, v109
	v_fmac_f32_e32 v98, v66, v110
	v_fmac_f32_e32 v99, v66, v111
	ds_read2st64_b32 v[100:101], v9 offset1:16
	ds_read2st64_b32 v[102:103], v9 offset0:32 offset1:48
	v_add_u32_e32 v9, 64, v9
	s_waitcnt vmcnt(29) lgkmcnt(10)
	v_fmac_f32_e32 v96, v67, v112
	v_fmac_f32_e32 v97, v67, v113
	v_fmac_f32_e32 v98, v67, v114
	v_fmac_f32_e32 v99, v67, v115
	ds_read2st64_b32 v[104:105], v9 offset1:16
	ds_read2st64_b32 v[106:107], v9 offset0:32 offset1:48
	v_add_u32_e32 v9, 64, v9
	s_waitcnt vmcnt(28) lgkmcnt(10)
	v_fmac_f32_e32 v96, v68, v116
	v_fmac_f32_e32 v97, v68, v117
	v_fmac_f32_e32 v98, v68, v118
	v_fmac_f32_e32 v99, v68, v119
	ds_read2st64_b32 v[108:109], v9 offset1:16
	ds_read2st64_b32 v[110:111], v9 offset0:32 offset1:48
	v_add_u32_e32 v9, 64, v9
	s_waitcnt vmcnt(27) lgkmcnt(10)
	v_fmac_f32_e32 v96, v69, v120
	v_fmac_f32_e32 v97, v69, v121
	v_fmac_f32_e32 v98, v69, v122
	v_fmac_f32_e32 v99, v69, v123
	ds_read2st64_b32 v[112:113], v9 offset1:16
	ds_read2st64_b32 v[114:115], v9 offset0:32 offset1:48
	v_add_u32_e32 v9, 64, v9
	s_waitcnt vmcnt(26) lgkmcnt(10)
	v_fmac_f32_e32 v96, v70, v124
	v_fmac_f32_e32 v97, v70, v125
	v_fmac_f32_e32 v98, v70, v126
	v_fmac_f32_e32 v99, v70, v127
	ds_read2st64_b32 v[116:117], v9 offset1:16
	ds_read2st64_b32 v[118:119], v9 offset0:32 offset1:48
	v_add_u32_e32 v9, 64, v9
	s_waitcnt vmcnt(25) lgkmcnt(10)
	v_fmac_f32_e32 v96, v71, v128
	v_fmac_f32_e32 v97, v71, v129
	v_fmac_f32_e32 v98, v71, v130
	v_fmac_f32_e32 v99, v71, v131
	ds_read2st64_b32 v[120:121], v9 offset1:16
	ds_read2st64_b32 v[122:123], v9 offset0:32 offset1:48
	v_add_u32_e32 v9, 64, v9
	s_waitcnt vmcnt(24) lgkmcnt(10)
	v_fmac_f32_e32 v96, v72, v100
	v_fmac_f32_e32 v97, v72, v101
	v_fmac_f32_e32 v98, v72, v102
	v_fmac_f32_e32 v99, v72, v103
	ds_read2st64_b32 v[124:125], v9 offset1:16
	ds_read2st64_b32 v[126:127], v9 offset0:32 offset1:48
	v_add_u32_e32 v9, 64, v9
	s_waitcnt vmcnt(23) lgkmcnt(10)
	v_fmac_f32_e32 v96, v73, v104
	v_fmac_f32_e32 v97, v73, v105
	v_fmac_f32_e32 v98, v73, v106
	v_fmac_f32_e32 v99, v73, v107
	ds_read2st64_b32 v[128:129], v9 offset1:16
	ds_read2st64_b32 v[130:131], v9 offset0:32 offset1:48
	v_add_u32_e32 v9, 64, v9
	s_waitcnt vmcnt(22) lgkmcnt(10)
; DI void phase_mod(const Params& p, int bid, int nb, char* lds) {
;     ...
;     for (int k = kg; k < 1024; k += 16) { const float w = p.w_ada[(size_t)k * 6144 + col]; a0 += sc[k] * w; a1 += sc[1024 + k] * w; a2 += sc[2048 + k] * w; a3 += sc[3072 + k] * w; }
;     part[(kg * 4 + 0) * 16 + cc] = a0; part[(kg * 4 + 1) * 16 + cc] = a1; part[(kg * 4 + 2) * 16 + cc] = a2; part[(kg * 4 + 3) * 16 + cc] = a3;
;     __syncthreads();
	v_fmac_f32_e32 v96, v74, v108
	v_fmac_f32_e32 v97, v74, v109
	v_fmac_f32_e32 v98, v74, v110
	v_fmac_f32_e32 v99, v74, v111
	ds_read2st64_b32 v[100:101], v9 offset1:16
	ds_read2st64_b32 v[102:103], v9 offset0:32 offset1:48
	v_add_u32_e32 v9, 64, v9
	s_waitcnt vmcnt(21) lgkmcnt(10)
	v_fmac_f32_e32 v96, v75, v112
	v_fmac_f32_e32 v97, v75, v113
	v_fmac_f32_e32 v98, v75, v114
	v_fmac_f32_e32 v99, v75, v115
	ds_read2st64_b32 v[104:105], v9 offset1:16
	ds_read2st64_b32 v[106:107], v9 offset0:32 offset1:48
	v_add_u32_e32 v9, 64, v9
	s_waitcnt vmcnt(20) lgkmcnt(10)
	v_fmac_f32_e32 v96, v76, v116
	v_fmac_f32_e32 v97, v76, v117
	v_fmac_f32_e32 v98, v76, v118
	v_fmac_f32_e32 v99, v76, v119
	ds_read2st64_b32 v[108:109], v9 offset1:16
	ds_read2st64_b32 v[110:111], v9 offset0:32 offset1:48
	v_add_u32_e32 v9, 64, v9
	s_waitcnt vmcnt(19) lgkmcnt(10)
	v_fmac_f32_e32 v96, v77, v120
	v_fmac_f32_e32 v97, v77, v121
	v_fmac_f32_e32 v98, v77, v122
	v_fmac_f32_e32 v99, v77, v123
	ds_read2st64_b32 v[112:113], v9 offset1:16
	ds_read2st64_b32 v[114:115], v9 offset0:32 offset1:48
	v_add_u32_e32 v9, 64, v9
	s_waitcnt vmcnt(18) lgkmcnt(10)
	v_fmac_f32_e32 v96, v78, v124
	v_fmac_f32_e32 v97, v78, v125
	v_fmac_f32_e32 v98, v78, v126
	v_fmac_f32_e32 v99, v78, v127
	ds_read2st64_b32 v[116:117], v9 offset1:16
	ds_read2st64_b32 v[118:119], v9 offset0:32 offset1:48
	v_add_u32_e32 v9, 64, v9
	s_waitcnt vmcnt(17) lgkmcnt(10)
	v_fmac_f32_e32 v96, v79, v128
	v_fmac_f32_e32 v97, v79, v129
	v_fmac_f32_e32 v98, v79, v130
	v_fmac_f32_e32 v99, v79, v131
	ds_read2st64_b32 v[120:121], v9 offset1:16
	ds_read2st64_b32 v[122:123], v9 offset0:32 offset1:48
	v_add_u32_e32 v9, 64, v9
	s_waitcnt vmcnt(16) lgkmcnt(10)
	v_fmac_f32_e32 v96, v80, v100
	v_fmac_f32_e32 v97, v80, v101
	v_fmac_f32_e32 v98, v80, v102
	v_fmac_f32_e32 v99, v80, v103
	ds_read2st64_b32 v[124:125], v9 offset1:16
	ds_read2st64_b32 v[126:127], v9 offset0:32 offset1:48
	v_add_u32_e32 v9, 64, v9
	s_waitcnt vmcnt(15) lgkmcnt(10)
	v_fmac_f32_e32 v96, v81, v104
	v_fmac_f32_e32 v97, v81, v105
	v_fmac_f32_e32 v98, v81, v106
	v_fmac_f32_e32 v99, v81, v107
	ds_read2st64_b32 v[128:129], v9 offset1:16
	ds_read2st64_b32 v[130:131], v9 offset0:32 offset1:48
	v_add_u32_e32 v9, 64, v9
	s_waitcnt vmcnt(14) lgkmcnt(10)
	v_fmac_f32_e32 v96, v82, v108
	v_fmac_f32_e32 v97, v82, v109
	v_fmac_f32_e32 v98, v82, v110
	v_fmac_f32_e32 v99, v82, v111
	ds_read2st64_b32 v[100:101], v9 offset1:16
	ds_read2st64_b32 v[102:103], v9 offset0:32 offset1:48
	v_add_u32_e32 v9, 64, v9
	s_waitcnt vmcnt(13) lgkmcnt(10)
	v_fmac_f32_e32 v96, v83, v112
	v_fmac_f32_e32 v97, v83, v113
	v_fmac_f32_e32 v98, v83, v114
	v_fmac_f32_e32 v99, v83, v115
	ds_read2st64_b32 v[104:105], v9 offset1:16
	ds_read2st64_b32 v[106:107], v9 offset0:32 offset1:48
	v_add_u32_e32 v9, 64, v9
	s_waitcnt vmcnt(12) lgkmcnt(10)
	v_fmac_f32_e32 v96, v84, v116
	v_fmac_f32_e32 v97, v84, v117
	v_fmac_f32_e32 v98, v84, v118
	v_fmac_f32_e32 v99, v84, v119
	ds_read2st64_b32 v[108:109], v9 offset1:16
	ds_read2st64_b32 v[110:111], v9 offset0:32 offset1:48
	v_add_u32_e32 v9, 64, v9
	s_waitcnt vmcnt(11) lgkmcnt(10)
	v_fmac_f32_e32 v96, v85, v120
	v_fmac_f32_e32 v97, v85, v121
	v_fmac_f32_e32 v98, v85, v122
	v_fmac_f32_e32 v99, v85, v123
	ds_read2st64_b32 v[112:113], v9 offset1:16
	ds_read2st64_b32 v[114:115], v9 offset0:32 offset1:48
	v_add_u32_e32 v9, 64, v9
	s_waitcnt vmcnt(10) lgkmcnt(10)
	v_fmac_f32_e32 v96, v86, v124
	v_fmac_f32_e32 v97, v86, v125
	v_fmac_f32_e32 v98, v86, v126
	v_fmac_f32_e32 v99, v86, v127
	ds_read2st64_b32 v[116:117], v9 offset1:16
	ds_read2st64_b32 v[118:119], v9 offset0:32 offset1:48
	v_add_u32_e32 v9, 64, v9
	s_waitcnt vmcnt(9) lgkmcnt(10)
	v_fmac_f32_e32 v96, v87, v128
	v_fmac_f32_e32 v97, v87, v129
	v_fmac_f32_e32 v98, v87, v130
	v_fmac_f32_e32 v99, v87, v131
	ds_read2st64_b32 v[120:121], v9 offset1:16
	ds_read2st64_b32 v[122:123], v9 offset0:32 offset1:48
	v_add_u32_e32 v9, 64, v9
	s_waitcnt vmcnt(8) lgkmcnt(10)
	v_fmac_f32_e32 v96, v88, v100
	v_fmac_f32_e32 v97, v88, v101
	v_fmac_f32_e32 v98, v88, v102
	v_fmac_f32_e32 v99, v88, v103
	ds_read2st64_b32 v[124:125], v9 offset1:16
	ds_read2st64_b32 v[126:127], v9 offset0:32 offset1:48
	v_add_u32_e32 v9, 64, v9
	s_waitcnt vmcnt(7) lgkmcnt(10)
	v_fmac_f32_e32 v96, v89, v104
	v_fmac_f32_e32 v97, v89, v105
	v_fmac_f32_e32 v98, v89, v106
	v_fmac_f32_e32 v99, v89, v107
	ds_read2st64_b32 v[128:129], v9 offset1:16
	ds_read2st64_b32 v[130:131], v9 offset0:32 offset1:48
	v_add_u32_e32 v9, 64, v9
	s_waitcnt vmcnt(6) lgkmcnt(10)
	v_fmac_f32_e32 v96, v90, v108
	v_fmac_f32_e32 v97, v90, v109
	v_fmac_f32_e32 v98, v90, v110
	v_fmac_f32_e32 v99, v90, v111
	s_waitcnt vmcnt(5) lgkmcnt(8)
	v_fmac_f32_e32 v96, v91, v112
	v_fmac_f32_e32 v97, v91, v113
	v_fmac_f32_e32 v98, v91, v114
	v_fmac_f32_e32 v99, v91, v115
	s_waitcnt vmcnt(4) lgkmcnt(6)
	v_fmac_f32_e32 v96, v92, v116
	v_fmac_f32_e32 v97, v92, v117
	v_fmac_f32_e32 v98, v92, v118
	v_fmac_f32_e32 v99, v92, v119
	s_waitcnt vmcnt(3) lgkmcnt(4)
	v_fmac_f32_e32 v96, v93, v120
	v_fmac_f32_e32 v97, v93, v121
	v_fmac_f32_e32 v98, v93, v122
	v_fmac_f32_e32 v99, v93, v123
	s_waitcnt vmcnt(2) lgkmcnt(2)
	v_fmac_f32_e32 v96, v94, v124
	v_fmac_f32_e32 v97, v94, v125
	v_fmac_f32_e32 v98, v94, v126
	v_fmac_f32_e32 v99, v94, v127
	s_waitcnt vmcnt(1) lgkmcnt(0)
	v_fmac_f32_e32 v96, v95, v128
	v_fmac_f32_e32 v97, v95, v129
	v_fmac_f32_e32 v98, v95, v130
	v_fmac_f32_e32 v99, v95, v131
	v_lshlrev_b32_e32 v11, 8, v3
	v_lshl_add_u32 v11, v2, 2, v11
	v_add3_u32 v11, v146, v11, 0
	v_add_u32_e32 v11, 0x4000, v11
	ds_write2_b32 v11, v96, v97 offset1:16
	ds_write2_b32 v11, v98, v99 offset0:32 offset1:48
	s_waitcnt lgkmcnt(0)
	s_barrier
; DI void phase_mod(const Params& p, int bid, int nb, char* lds) {
;     ...
;     if (tid < 64) { const int b = tid >> 4; float s = 0.f;
; #pragma unroll
;       for (int q = 0; q < 16; ++q) s += part[(q * 4 + b) * 16 + cc];
;       mod[b * 6144 + col] = s + p.b_ada[col]; }
;     __syncthreads();
	v_cmp_gt_i32_e32 vcc, 64, v1
	s_and_saveexec_b64 s[10:11], vcc
	s_cbranch_execz .Lmod_done
	v_lshl_add_u32 v9, v1, 2, v146
	ds_read2st64_b32 v[100:101], v9 offset0:64 offset1:65
	ds_read2st64_b32 v[102:103], v9 offset0:66 offset1:67
	ds_read2st64_b32 v[104:105], v9 offset0:68 offset1:69
	ds_read2st64_b32 v[106:107], v9 offset0:70 offset1:71
	ds_read2st64_b32 v[108:109], v9 offset0:72 offset1:73
	ds_read2st64_b32 v[110:111], v9 offset0:74 offset1:75
	ds_read2st64_b32 v[112:113], v9 offset0:76 offset1:77
	ds_read2st64_b32 v[114:115], v9 offset0:78 offset1:79
	s_waitcnt lgkmcnt(7)
	v_add_f32_e32 v132, 0, v100
	v_add_f32_e32 v132, v132, v101
	s_waitcnt lgkmcnt(6)
	v_add_f32_e32 v132, v132, v102
	v_add_f32_e32 v132, v132, v103
	s_waitcnt lgkmcnt(5)
	v_add_f32_e32 v132, v132, v104
	v_add_f32_e32 v132, v132, v105
	s_waitcnt lgkmcnt(4)
	v_add_f32_e32 v132, v132, v106
	v_add_f32_e32 v132, v132, v107
	s_waitcnt lgkmcnt(3)
	v_add_f32_e32 v132, v132, v108
	v_add_f32_e32 v132, v132, v109
	s_waitcnt lgkmcnt(2)
	v_add_f32_e32 v132, v132, v110
	v_add_f32_e32 v132, v132, v111
	s_waitcnt lgkmcnt(1)
	v_add_f32_e32 v132, v132, v112
	v_add_f32_e32 v132, v132, v113
	s_waitcnt lgkmcnt(0)
	v_add_f32_e32 v132, v132, v114
	v_add_f32_e32 v132, v132, v115
	v_mul_u32_u24_e32 v7, 0x6000, v3
	v_lshl_add_u32 v7, v4, 2, v7
	s_waitcnt vmcnt(0)
	v_add_f32_e32 v132, v132, v10
	global_store_dword v7, v132, s[14:15]
.Lmod_done:
	s_or_b64 exec, exec, s[10:11]
	s_barrier
